# FFN-in fp8 phase: sixth-round units split in two row halves across CU c and c+128, PP tail units dealt one per CU
# baseline (speedup 1.0000x reference)
.LBB0_210:
	s_cmp_eq_u32 s56, 1
	v_readlane_b32 s0, v254, 27
	s_cselect_b64 s[42:43], -1, 0
	v_readlane_b32 s1, v254, 28
	s_or_b64 s[0:1], s[0:1], s[42:43]
	v_readfirstlane_b32 s2, v0
	v_cndmask_b32_e64 v0, 0, 1, s[0:1]
	s_nop 0
	v_readfirstlane_b32 s0, v0
	s_bitcmp1_b32 s0, 0
	s_cselect_b64 s[0:1], -1, 0
	v_writelane_b32 v254, s0, 14
	s_cmp_gt_u32 s83, 3
	s_nop 0
	v_writelane_b32 v254, s1, 15
	s_cselect_b64 s[0:1], -1, 0
	v_cndmask_b32_e64 v0, 0, 1, s[0:1]
	s_nop 0
	v_readfirstlane_b32 s0, v0
	s_bitcmp1_b32 s0, 0
	s_cselect_b64 s[0:1], -1, 0
	v_writelane_b32 v254, s0, 50
	s_cmp_eq_u32 s2, 0
	s_cselect_b64 s[26:27], -1, 0
	v_writelane_b32 v254, s1, 51
	s_cmp_lg_u32 s2, 0
	v_readlane_b32 s0, v254, 7
	v_readlane_b32 s2, v254, 41
	s_cselect_b64 s[18:19], -1, 0
	v_readlane_b32 s1, v254, 8
	s_cmp_ge_i32 s2, s0
	s_cselect_b64 s[4:5], -1, 0
	s_cmp_lt_i32 s2, s1
	s_cselect_b64 s[0:1], -1, 0
	s_and_b64 s[0:1], s[4:5], s[0:1]
	v_writelane_b32 v254, s83, 16
	s_andn2_b64 vcc, exec, s[0:1]
	v_writelane_b32 v254, s85, 35
	s_cbranch_vccnz .LBB0_270
	s_mov_b32 s41, 1
	s_cmp_lt_i32 s41, 1
	s_cbranch_scc1 .LBB0_270
	v_writelane_b32 v254, s4, 52
	s_mov_b32 s57, s77
	s_mov_b32 s59, 0
	v_writelane_b32 v254, s5, 53
	v_writelane_b32 v254, s26, 54
	s_mov_b32 s51, s77
	s_nop 0
	v_writelane_b32 v254, s27, 55
	v_writelane_b32 v254, s42, 56
	s_nop 1
	v_writelane_b32 v254, s43, 57
	s_nop 0
	v_readlane_b32 s9, v254, 31
	s_cmpk_lt_u32 s9, 0x580
	s_cselect_b64 s[0:1], -1, 0
	s_cmp_eq_u32 s36, 0
	s_cselect_b64 s[16:17], -1, 0
	s_and_b64 s[2:3], s[16:17], exec
	v_writelane_b32 v254, s36, 58
	s_cselect_b32 s2, 0, 0x4200000
	v_writelane_b32 v254, s2, 33
	s_mov_b32 s2, 0x4f200000
	s_cselect_b32 s2, s2, 0x4e200000
	v_writelane_b32 v254, s2, 39
	s_and_b32 s2, s9, 7
	s_lshr_b32 s3, s9, 3
	s_mulk_i32 s2, 0xb0
	s_add_i32 s2, s2, s3
	s_mul_hi_u32 s3, s2, 0xba2e8c
	s_mul_i32 s4, s3, 0xfffffea0
	s_add_i32 s4, s4, s2
	s_lshl_b32 s2, s3, 3
	s_bfe_u32 s3, s9, 0x30003
	s_lshr_b32 s45, s4, 3
	s_or_b32 s44, s2, s3
	s_lshl_b32 s46, s45, 19
	s_or_b32 s2, s46, 0x40000
	s_lshl_b32 s48, s44, 19
	v_writelane_b32 v254, s2, 29
	s_or_b32 s2, s48, 0x40000
	s_or_b32 s50, s46, 0x80
	s_or_b32 s47, s46, 0x40080
	v_writelane_b32 v254, s2, 17
	s_and_b64 s[2:3], s[16:17], exec
	s_mov_b32 s2, 0x4c100000
	s_cselect_b32 s2, s2, 0x32e00000
	v_writelane_b32 v254, s2, 19
	s_mov_b64 s[4:5], s[56:57]
	v_readlane_b32 s2, v254, 37
	s_mov_b32 s8, s2
	s_abs_i32 s2, s2
	v_cvt_f32_u32_e32 v0, s2
	s_mov_b32 s56, s4
	s_lshl_b64 s[4:5], s[4:5], 22
	v_readlane_b32 s3, v254, 38
	v_rcp_iflag_f32_e32 v0, v0
	v_writelane_b32 v254, s4, 12
	s_sub_i32 s3, 0, s2
	s_lshl_b32 s53, s45, 20
	v_mul_f32_e32 v0, 0x4f7ffffe, v0
	v_cvt_u32_f32_e32 v0, v0
	v_writelane_b32 v254, s5, 13
	s_lshl_b32 s55, s44, 20
	s_or_b32 s54, s53, 0x80000
	v_readfirstlane_b32 s4, v0
	s_mul_i32 s3, s3, s4
	s_mul_hi_u32 s3, s4, s3
	s_add_i32 s4, s4, s3
	s_mul_hi_u32 s3, s4, 0x580
	s_mul_i32 s3, s3, s2
	s_sub_i32 s3, 0x580, s3
	s_or_b32 s57, s55, 0x80000
	s_or_b32 s49, s53, 0x80
	s_or_b32 s58, s53, 0x80080
	s_sub_i32 s4, s3, s2
	s_cmp_ge_u32 s3, s2
	s_cselect_b32 s3, s4, s3
	s_sub_i32 s4, s3, s2
	s_cmp_ge_u32 s3, s2
	s_cselect_b32 s6, s4, s3
	s_sub_i32 s2, s8, s6
	s_abs_i32 s3, s2
	v_cvt_f32_u32_e32 v0, s3
	s_sub_i32 s5, 0, s3
	s_add_i32 s4, s2, 0xff
	s_xor_b32 s2, s4, s2
	v_rcp_iflag_f32_e32 v0, v0
	s_abs_i32 s4, s4
	s_ashr_i32 s2, s2, 31
	v_mul_f32_e32 v0, 0x4f7ffffe, v0
	v_cvt_u32_f32_e32 v0, v0
	s_nop 0
	v_readfirstlane_b32 s7, v0
	s_mul_i32 s5, s5, s7
	s_mul_hi_u32 s5, s7, s5
	s_add_i32 s7, s7, s5
	s_mul_hi_u32 s5, s4, s7
	s_mul_i32 s7, s5, s3
	s_sub_i32 s4, s4, s7
	s_add_i32 s7, s5, 1
	s_sub_i32 s8, s4, s3
	s_cmp_ge_u32 s4, s3
	s_cselect_b32 s5, s7, s5
	s_cselect_b32 s4, s8, s4
	s_add_i32 s7, s5, 1
	s_cmp_ge_u32 s4, s3
	s_cselect_b32 s3, s7, s5
	s_xor_b32 s3, s3, s2
	s_sub_i32 s60, s3, s2
	v_readlane_b32 s98, v254, 37
	s_cmp_eq_u32 s98, 0x100
	s_cselect_b32 s6, 0, s6
	s_cselect_b32 s60, 1, s60
	s_cmp_ge_i32 s9, s6
	s_cselect_b64 s[2:3], -1, 0
	s_cmp_gt_i32 s60, 0
	s_cselect_b64 s[4:5], -1, 0
	s_and_b64 s[24:25], s[2:3], s[4:5]
	s_sub_i32 s2, s9, s6
	s_mul_i32 s61, s60, s2
	s_cmpk_lt_i32 s61, 0x100
	s_cselect_b64 s[2:3], -1, 0
	v_writelane_b32 v254, s2, 21
	v_cndmask_b32_e64 v0, 0, 1, s[0:1]
	s_nop 0
	v_writelane_b32 v254, s3, 22
	s_ashr_i32 s2, s61, 3
	v_writelane_b32 v254, s2, 23
	s_and_b32 s2, s61, 7
	v_writelane_b32 v254, s2, 25
	s_branch .LBB0_215

.LBB0_222:
	v_readlane_b32 s6, v254, 37
	s_add_i32 s83, s83, 1
	v_readlane_b32 s7, v254, 38
	s_mul_i32 s6, s83, s6
	v_readlane_b32 s7, v254, 31
	s_add_i32 s6, s6, s7
	v_readlane_b32 s98, v254, 37
	s_cmp_eq_u32 s98, 0x100
	s_cselect_b32 s98, 1, 0
	s_lshr_b32 s99, s7, 7
	s_add_i32 s99, s99, 1
	s_cmp_eq_u32 s83, 6
	s_cselect_b32 s32, s99, 0
	s_mul_i32 s32, s32, s98
	s_cmp_eq_u32 s83, 5
	s_cselect_b32 s99, 0x80, 0
	s_mul_i32 s99, s99, s98
	s_andn2_b32 s6, s6, s99
	s_cmpk_lt_u32 s6, 0x580
	s_cselect_b64 s[38:39], -1, 0
	s_cmpk_gt_u32 s6, 0x57f
	s_cbranch_scc1 .LBB0_224
	s_and_b32 s7, s6, 7
	s_lshr_b32 s14, s6, 3
	s_mulk_i32 s7, 0xb0
	s_add_i32 s7, s7, s14
	s_mul_hi_u32 s14, s7, 0xba2e8c
	s_mul_i32 s15, s14, 0xfffffea0
	s_add_i32 s15, s15, s7
	s_lshl_b32 s7, s14, 3
	s_bfe_u32 s6, s6, 0x30003
	s_or_b32 s85, s7, s6
	s_lshr_b32 s22, s15, 3
.LBB0_224:
	ds_read_b128 v[2:5], v169
	ds_read_b128 v[6:9], v169 offset:1024
	ds_read_b128 v[10:13], v169 offset:2048
	ds_read_b128 v[14:17], v169 offset:3072
	ds_read_b128 v[18:21], v170
	ds_read_b128 v[22:25], v170 offset:1024
	ds_read_b128 v[26:29], v170 offset:2048
	ds_read_b128 v[30:33], v170 offset:3072
	s_lshl_b32 s43, s85, 19
	s_lshl_b32 s52, s22, 19
	s_or_b32 s15, s29, 0x80
	s_or_b32 s62, s28, 0x100
	s_and_b64 s[6:7], s[38:39], exec
	s_cselect_b32 vcc_lo, s43, s29
	s_or_b32 s14, s29, 0x100
	s_and_b64 s[6:7], s[38:39], exec
	s_cselect_b32 vcc_hi, s52, s28
	s_mov_b32 m0, s79
	ds_read_b128 v[34:37], v171
	ds_read_b128 v[38:41], v171 offset:1024
	ds_read_b128 v[42:45], v171 offset:2048
	ds_read_b128 v[46:49], v171 offset:3072
	ds_read_b128 v[50:53], v171 offset:4096
	ds_read_b128 v[54:57], v171 offset:5120
	ds_read_b128 v[58:61], v171 offset:6144
	ds_read_b128 v[62:65], v171 offset:7168
	buffer_load_dwordx4 v163, s[64:67], s15 offen lds
	s_mov_b32 m0, s81
	s_or_b32 s6, s29, 0x40080
	buffer_load_dwordx4 v165, s[64:67], s15 offen lds
	s_mov_b32 m0, s80
	s_nop 0
	buffer_load_dwordx4 v163, s[64:67], s6 offen lds
	s_mov_b32 m0, s82
	s_nop 0
	buffer_load_dwordx4 v165, s[64:67], s6 offen lds
	s_waitcnt vmcnt(8)
	s_waitcnt lgkmcnt(0)
	s_barrier
	s_setprio 1
	s_cmp_eq_u32 s32, 2
	s_cbranch_scc1 .Lhk_0
	s_waitcnt lgkmcnt(6)
	v_mfma_scale_f32_16x16x128_f8f6f4 v[150:153], v[2:9], v[34:41], 0, v234, v234 op_sel_hi:[0,0,0]
	v_mfma_scale_f32_16x16x128_f8f6f4 v[146:149], v[10:17], v[34:41], 0, v234, v234 op_sel_hi:[0,0,0]
	s_waitcnt vmcnt(17) lgkmcnt(4)
	v_mfma_scale_f32_16x16x128_f8f6f4 v[134:137], v[2:9], v[42:49], 0, v234, v234 op_sel_hi:[0,0,0]
	v_mfma_scale_f32_16x16x128_f8f6f4 v[130:133], v[10:17], v[42:49], 0, v234, v234 op_sel_hi:[0,0,0]
	s_waitcnt lgkmcnt(2)
	v_mfma_scale_f32_16x16x128_f8f6f4 v[118:121], v[2:9], v[50:57], 0, v234, v234 op_sel_hi:[0,0,0]
	v_mfma_scale_f32_16x16x128_f8f6f4 v[114:117], v[10:17], v[50:57], 0, v234, v234 op_sel_hi:[0,0,0]
	s_waitcnt lgkmcnt(0)
	v_mfma_scale_f32_16x16x128_f8f6f4 v[98:101], v[2:9], v[58:65], 0, v234, v234 op_sel_hi:[0,0,0]
	v_mfma_scale_f32_16x16x128_f8f6f4 v[90:93], v[10:17], v[58:65], 0, v234, v234 op_sel_hi:[0,0,0]
	v_mfma_scale_f32_16x16x128_f8f6f4 v[158:161], v[18:25], v[34:41], 0, v234, v234 op_sel_hi:[0,0,0]
	v_mfma_scale_f32_16x16x128_f8f6f4 v[154:157], v[26:33], v[34:41], 0, v234, v234 op_sel_hi:[0,0,0]
	v_mfma_scale_f32_16x16x128_f8f6f4 v[142:145], v[18:25], v[42:49], 0, v234, v234 op_sel_hi:[0,0,0]
	s_waitcnt vmcnt(16)
	v_mfma_scale_f32_16x16x128_f8f6f4 v[138:141], v[26:33], v[42:49], 0, v234, v234 op_sel_hi:[0,0,0]
	v_mfma_scale_f32_16x16x128_f8f6f4 v[126:129], v[18:25], v[50:57], 0, v234, v234 op_sel_hi:[0,0,0]
	v_mfma_scale_f32_16x16x128_f8f6f4 v[122:125], v[26:33], v[50:57], 0, v234, v234 op_sel_hi:[0,0,0]
	v_mfma_scale_f32_16x16x128_f8f6f4 v[110:113], v[18:25], v[58:65], 0, v234, v234 op_sel_hi:[0,0,0]
	v_mfma_scale_f32_16x16x128_f8f6f4 v[106:109], v[26:33], v[58:65], 0, v234, v234 op_sel_hi:[0,0,0]
.Lhk_0:
	s_setprio 0
	s_barrier
	s_mov_b32 m0, s9
	s_mov_b32 s6, s66
	s_mov_b32 s7, s67
	ds_read_b128 v[74:77], v171 offset:16384
	ds_read_b128 v[78:81], v171 offset:17408
	ds_read_b128 v[174:177], v171 offset:18432
	ds_read_b128 v[178:181], v171 offset:19456
	ds_read_b128 v[182:185], v171 offset:20480
	ds_read_b128 v[186:189], v171 offset:21504
	ds_read_b128 v[190:193], v171 offset:22528
	ds_read_b128 v[194:197], v171 offset:23552
	buffer_load_dwordx4 v164, s[4:7], s62 offen lds
	s_mov_b32 m0, s10
	s_or_b32 s15, s28, 0x40100
	buffer_load_dwordx4 v166, s[4:7], s62 offen lds
	s_mov_b32 m0, s11
	s_nop 0
	buffer_load_dwordx4 v164, s[4:7], s15 offen lds
	s_mov_b32 m0, s12
	s_nop 0
	buffer_load_dwordx4 v166, s[4:7], s15 offen lds
	s_waitcnt vmcnt(6)
	s_waitcnt lgkmcnt(0)
	s_barrier
	s_setprio 1
	s_cmp_eq_u32 s32, 1
	s_cbranch_scc1 .Lhk_1
	s_waitcnt lgkmcnt(6)
	v_mfma_scale_f32_16x16x128_f8f6f4 v[86:89], v[2:9], v[74:81], 0, v234, v234 op_sel_hi:[0,0,0]
	v_mfma_scale_f32_16x16x128_f8f6f4 v[82:85], v[10:17], v[74:81], 0, v234, v234 op_sel_hi:[0,0,0]
	s_waitcnt lgkmcnt(4)
	v_mfma_scale_f32_16x16x128_f8f6f4 v[70:73], v[2:9], v[174:181], 0, v234, v234 op_sel_hi:[0,0,0]
	v_mfma_scale_f32_16x16x128_f8f6f4 v[66:69], v[10:17], v[174:181], 0, v234, v234 op_sel_hi:[0,0,0]
	s_waitcnt lgkmcnt(2)
	v_mfma_scale_f32_16x16x128_f8f6f4 v[58:61], v[2:9], v[182:189], 0, v234, v234 op_sel_hi:[0,0,0]
	v_mfma_scale_f32_16x16x128_f8f6f4 v[50:53], v[10:17], v[182:189], 0, v234, v234 op_sel_hi:[0,0,0]
	s_waitcnt lgkmcnt(0)
	v_mfma_scale_f32_16x16x128_f8f6f4 v[42:45], v[2:9], v[190:197], 0, v234, v234 op_sel_hi:[0,0,0]
	v_mfma_scale_f32_16x16x128_f8f6f4 v[34:37], v[10:17], v[190:197], 0, v234, v234 op_sel_hi:[0,0,0]
	v_mfma_scale_f32_16x16x128_f8f6f4 v[102:105], v[18:25], v[74:81], 0, v234, v234 op_sel_hi:[0,0,0]
	v_mfma_scale_f32_16x16x128_f8f6f4 v[94:97], v[26:33], v[74:81], 0, v234, v234 op_sel_hi:[0,0,0]
	v_mfma_scale_f32_16x16x128_f8f6f4 v[78:81], v[18:25], v[174:181], 0, v234, v234 op_sel_hi:[0,0,0]
	v_mfma_scale_f32_16x16x128_f8f6f4 v[74:77], v[26:33], v[174:181], 0, v234, v234 op_sel_hi:[0,0,0]
	v_mfma_scale_f32_16x16x128_f8f6f4 v[62:65], v[18:25], v[182:189], 0, v234, v234 op_sel_hi:[0,0,0]
	v_mfma_scale_f32_16x16x128_f8f6f4 v[54:57], v[26:33], v[182:189], 0, v234, v234 op_sel_hi:[0,0,0]
	v_mfma_scale_f32_16x16x128_f8f6f4 v[46:49], v[18:25], v[190:197], 0, v234, v234 op_sel_hi:[0,0,0]
	v_mfma_scale_f32_16x16x128_f8f6f4 v[38:41], v[26:33], v[190:197], 0, v234, v234 op_sel_hi:[0,0,0]
.Lhk_1:
	s_setprio 0
	s_barrier
	ds_read_b128 v[26:29], v172
	ds_read_b128 v[30:33], v172 offset:1024
	ds_read_b128 v[18:21], v172 offset:2048
	ds_read_b128 v[22:25], v172 offset:3072
	ds_read_b128 v[10:13], v173
	ds_read_b128 v[14:17], v173 offset:1024
	ds_read_b128 v[2:5], v173 offset:2048
	ds_read_b128 v[6:9], v173 offset:3072
	s_mov_b32 m0, s8
	ds_read_b128 v[174:177], v171 offset:32768
	ds_read_b128 v[178:181], v171 offset:33792
	ds_read_b128 v[182:185], v171 offset:34816
	ds_read_b128 v[186:189], v171 offset:35840
	ds_read_b128 v[190:193], v171 offset:36864
	ds_read_b128 v[194:197], v171 offset:37888
	ds_read_b128 v[204:207], v171 offset:38912
	ds_read_b128 v[208:211], v171 offset:39936
	buffer_load_dwordx4 v163, s[64:67], s14 offen lds
	s_mov_b32 m0, s13
	s_nop 0
	buffer_load_dwordx4 v165, s[64:67], s14 offen lds
	s_or_b32 s14, s29, 0x40100
	s_mov_b32 m0, s20
	s_nop 0
	buffer_load_dwordx4 v163, s[64:67], s14 offen lds
	s_mov_b32 m0, s21
	s_nop 0
	buffer_load_dwordx4 v165, s[64:67], s14 offen lds
	s_waitcnt vmcnt(8)
	s_waitcnt lgkmcnt(0)
	s_barrier
	s_setprio 1
	s_cmp_eq_u32 s32, 2
	s_cbranch_scc1 .Lhk_2
	s_waitcnt lgkmcnt(6)
	v_mfma_scale_f32_16x16x128_f8f6f4 v[150:153], v[26:33], v[174:181], v[150:153], v234, v234 op_sel_hi:[0,0,0]
	v_mfma_scale_f32_16x16x128_f8f6f4 v[146:149], v[18:25], v[174:181], v[146:149], v234, v234 op_sel_hi:[0,0,0]
	s_waitcnt lgkmcnt(4)
	v_mfma_scale_f32_16x16x128_f8f6f4 v[134:137], v[26:33], v[182:189], v[134:137], v234, v234 op_sel_hi:[0,0,0]
	v_mfma_scale_f32_16x16x128_f8f6f4 v[130:133], v[18:25], v[182:189], v[130:133], v234, v234 op_sel_hi:[0,0,0]
	s_waitcnt lgkmcnt(2)
	v_mfma_scale_f32_16x16x128_f8f6f4 v[118:121], v[26:33], v[190:197], v[118:121], v234, v234 op_sel_hi:[0,0,0]
	v_mfma_scale_f32_16x16x128_f8f6f4 v[114:117], v[18:25], v[190:197], v[114:117], v234, v234 op_sel_hi:[0,0,0]
	s_waitcnt lgkmcnt(0)
	v_mfma_scale_f32_16x16x128_f8f6f4 v[98:101], v[26:33], v[204:211], v[98:101], v234, v234 op_sel_hi:[0,0,0]
	v_mfma_scale_f32_16x16x128_f8f6f4 v[90:93], v[18:25], v[204:211], v[90:93], v234, v234 op_sel_hi:[0,0,0]
	v_mfma_scale_f32_16x16x128_f8f6f4 v[158:161], v[10:17], v[174:181], v[158:161], v234, v234 op_sel_hi:[0,0,0]
	v_mfma_scale_f32_16x16x128_f8f6f4 v[154:157], v[2:9], v[174:181], v[154:157], v234, v234 op_sel_hi:[0,0,0]
	v_mfma_scale_f32_16x16x128_f8f6f4 v[142:145], v[10:17], v[182:189], v[142:145], v234, v234 op_sel_hi:[0,0,0]
	v_mfma_scale_f32_16x16x128_f8f6f4 v[138:141], v[2:9], v[182:189], v[138:141], v234, v234 op_sel_hi:[0,0,0]
	v_mfma_scale_f32_16x16x128_f8f6f4 v[126:129], v[10:17], v[190:197], v[126:129], v234, v234 op_sel_hi:[0,0,0]
	v_mfma_scale_f32_16x16x128_f8f6f4 v[122:125], v[2:9], v[190:197], v[122:125], v234, v234 op_sel_hi:[0,0,0]
	v_mfma_scale_f32_16x16x128_f8f6f4 v[110:113], v[10:17], v[204:211], v[110:113], v234, v234 op_sel_hi:[0,0,0]
	v_mfma_scale_f32_16x16x128_f8f6f4 v[106:109], v[2:9], v[204:211], v[106:109], v234, v234 op_sel_hi:[0,0,0]
.Lhk_2:
	s_setprio 0
	s_barrier
	s_mov_b32 m0, s26
	s_or_b32 s14, s28, 0x180
	ds_read_b128 v[174:177], v171 offset:49152
	ds_read_b128 v[178:181], v171 offset:50176
	ds_read_b128 v[182:185], v171 offset:51200
	ds_read_b128 v[186:189], v171 offset:52224
	ds_read_b128 v[190:193], v171 offset:53248
	ds_read_b128 v[194:197], v171 offset:54272
	ds_read_b128 v[204:207], v171 offset:55296
	ds_read_b128 v[208:211], v171 offset:56320
	buffer_load_dwordx4 v164, s[4:7], s14 offen lds
	s_mov_b32 m0, s27
	s_nop 0
	buffer_load_dwordx4 v166, s[4:7], s14 offen lds
	s_or_b32 s14, s28, 0x40180
	s_mov_b32 m0, s40
	s_nop 0
	buffer_load_dwordx4 v164, s[4:7], s14 offen lds
	s_mov_b32 m0, s76
	s_nop 0
	buffer_load_dwordx4 v166, s[4:7], s14 offen lds
	s_waitcnt vmcnt(6)
	s_waitcnt lgkmcnt(0)
	s_barrier
	s_setprio 1
	s_cmp_eq_u32 s32, 1
	s_cbranch_scc1 .Lhk_3
	s_waitcnt lgkmcnt(6)
	v_mfma_scale_f32_16x16x128_f8f6f4 v[86:89], v[26:33], v[174:181], v[86:89], v234, v234 op_sel_hi:[0,0,0]
	v_mfma_scale_f32_16x16x128_f8f6f4 v[82:85], v[18:25], v[174:181], v[82:85], v234, v234 op_sel_hi:[0,0,0]
	s_waitcnt lgkmcnt(4)
	v_mfma_scale_f32_16x16x128_f8f6f4 v[70:73], v[26:33], v[182:189], v[70:73], v234, v234 op_sel_hi:[0,0,0]
	v_mfma_scale_f32_16x16x128_f8f6f4 v[66:69], v[18:25], v[182:189], v[66:69], v234, v234 op_sel_hi:[0,0,0]
	s_waitcnt lgkmcnt(2)
	v_mfma_scale_f32_16x16x128_f8f6f4 v[58:61], v[26:33], v[190:197], v[58:61], v234, v234 op_sel_hi:[0,0,0]
	v_mfma_scale_f32_16x16x128_f8f6f4 v[50:53], v[18:25], v[190:197], v[50:53], v234, v234 op_sel_hi:[0,0,0]
	s_waitcnt lgkmcnt(0)
	v_mfma_scale_f32_16x16x128_f8f6f4 v[42:45], v[26:33], v[204:211], v[42:45], v234, v234 op_sel_hi:[0,0,0]
	v_mfma_scale_f32_16x16x128_f8f6f4 v[34:37], v[18:25], v[204:211], v[34:37], v234, v234 op_sel_hi:[0,0,0]
	v_mfma_scale_f32_16x16x128_f8f6f4 v[102:105], v[10:17], v[174:181], v[102:105], v234, v234 op_sel_hi:[0,0,0]
	v_mfma_scale_f32_16x16x128_f8f6f4 v[94:97], v[2:9], v[174:181], v[94:97], v234, v234 op_sel_hi:[0,0,0]
	v_mfma_scale_f32_16x16x128_f8f6f4 v[78:81], v[10:17], v[182:189], v[78:81], v234, v234 op_sel_hi:[0,0,0]
	v_mfma_scale_f32_16x16x128_f8f6f4 v[74:77], v[2:9], v[182:189], v[74:77], v234, v234 op_sel_hi:[0,0,0]
	v_mfma_scale_f32_16x16x128_f8f6f4 v[62:65], v[10:17], v[190:197], v[62:65], v234, v234 op_sel_hi:[0,0,0]
	v_mfma_scale_f32_16x16x128_f8f6f4 v[54:57], v[2:9], v[190:197], v[54:57], v234, v234 op_sel_hi:[0,0,0]
	v_mfma_scale_f32_16x16x128_f8f6f4 v[46:49], v[10:17], v[204:211], v[46:49], v234, v234 op_sel_hi:[0,0,0]
	v_mfma_scale_f32_16x16x128_f8f6f4 v[38:41], v[2:9], v[204:211], v[38:41], v234, v234 op_sel_hi:[0,0,0]
.Lhk_3:
	s_setprio 0
	s_barrier
	s_addk_i32 s28, 0x200
	s_add_i32 s29, s29, 0x40180
	s_mov_b32 s62, 0
.LBB0_225:
	ds_read_b128 v[2:5], v169
	ds_read_b128 v[6:9], v169 offset:1024
	ds_read_b128 v[10:13], v169 offset:2048
	ds_read_b128 v[14:17], v169 offset:3072
	ds_read_b128 v[18:21], v170
	ds_read_b128 v[22:25], v170 offset:1024
	ds_read_b128 v[26:29], v170 offset:2048
	ds_read_b128 v[30:33], v170 offset:3072
	s_add_i32 s15, s29, 0xfffc0080
	s_cmp_eq_u32 s62, 12
	s_cselect_b32 s14, vcc_hi, s28
	s_cselect_b32 s15, vcc_lo, s15
	s_add_i32 s63, s29, 0xfffc0000
	s_mov_b32 m0, s79
	ds_read_b128 v[174:177], v171
	ds_read_b128 v[178:181], v171 offset:1024
	ds_read_b128 v[182:185], v171 offset:2048
	ds_read_b128 v[186:189], v171 offset:3072
	ds_read_b128 v[190:193], v171 offset:4096
	ds_read_b128 v[194:197], v171 offset:5120
	ds_read_b128 v[204:207], v171 offset:6144
	ds_read_b128 v[208:211], v171 offset:7168
	buffer_load_dwordx4 v163, s[64:67], s63 offen lds
	s_mov_b32 m0, s81
	s_nop 0
	buffer_load_dwordx4 v165, s[64:67], s63 offen lds
	s_mov_b32 m0, s80
	s_nop 0
	buffer_load_dwordx4 v163, s[64:67], s29 offen lds
	s_mov_b32 m0, s82
	s_nop 0
	buffer_load_dwordx4 v165, s[64:67], s29 offen lds
	s_waitcnt vmcnt(8)
	s_waitcnt lgkmcnt(0)
	s_barrier
	s_setprio 1
	s_cmp_eq_u32 s32, 2
	s_cbranch_scc1 .Lhk_4
	s_waitcnt lgkmcnt(6)
	v_mfma_scale_f32_16x16x128_f8f6f4 v[150:153], v[2:9], v[174:181], v[150:153], v234, v234 op_sel_hi:[0,0,0]
	v_mfma_scale_f32_16x16x128_f8f6f4 v[146:149], v[10:17], v[174:181], v[146:149], v234, v234 op_sel_hi:[0,0,0]
	s_waitcnt lgkmcnt(4)
	v_mfma_scale_f32_16x16x128_f8f6f4 v[134:137], v[2:9], v[182:189], v[134:137], v234, v234 op_sel_hi:[0,0,0]
	v_mfma_scale_f32_16x16x128_f8f6f4 v[130:133], v[10:17], v[182:189], v[130:133], v234, v234 op_sel_hi:[0,0,0]
	s_waitcnt lgkmcnt(2)
	v_mfma_scale_f32_16x16x128_f8f6f4 v[118:121], v[2:9], v[190:197], v[118:121], v234, v234 op_sel_hi:[0,0,0]
	v_mfma_scale_f32_16x16x128_f8f6f4 v[114:117], v[10:17], v[190:197], v[114:117], v234, v234 op_sel_hi:[0,0,0]
	s_waitcnt lgkmcnt(0)
	v_mfma_scale_f32_16x16x128_f8f6f4 v[98:101], v[2:9], v[204:211], v[98:101], v234, v234 op_sel_hi:[0,0,0]
	v_mfma_scale_f32_16x16x128_f8f6f4 v[90:93], v[10:17], v[204:211], v[90:93], v234, v234 op_sel_hi:[0,0,0]
	v_mfma_scale_f32_16x16x128_f8f6f4 v[158:161], v[18:25], v[174:181], v[158:161], v234, v234 op_sel_hi:[0,0,0]
	v_mfma_scale_f32_16x16x128_f8f6f4 v[154:157], v[26:33], v[174:181], v[154:157], v234, v234 op_sel_hi:[0,0,0]
	v_mfma_scale_f32_16x16x128_f8f6f4 v[142:145], v[18:25], v[182:189], v[142:145], v234, v234 op_sel_hi:[0,0,0]
	v_mfma_scale_f32_16x16x128_f8f6f4 v[138:141], v[26:33], v[182:189], v[138:141], v234, v234 op_sel_hi:[0,0,0]
	v_mfma_scale_f32_16x16x128_f8f6f4 v[126:129], v[18:25], v[190:197], v[126:129], v234, v234 op_sel_hi:[0,0,0]
	v_mfma_scale_f32_16x16x128_f8f6f4 v[122:125], v[26:33], v[190:197], v[122:125], v234, v234 op_sel_hi:[0,0,0]
	v_mfma_scale_f32_16x16x128_f8f6f4 v[110:113], v[18:25], v[204:211], v[110:113], v234, v234 op_sel_hi:[0,0,0]
	v_mfma_scale_f32_16x16x128_f8f6f4 v[106:109], v[26:33], v[204:211], v[106:109], v234, v234 op_sel_hi:[0,0,0]
.Lhk_4:
	s_setprio 0
	s_barrier
	s_mov_b32 m0, s9
	ds_read_b128 v[174:177], v171 offset:16384
	ds_read_b128 v[178:181], v171 offset:17408
	ds_read_b128 v[182:185], v171 offset:18432
	ds_read_b128 v[186:189], v171 offset:19456
	ds_read_b128 v[190:193], v171 offset:20480
	ds_read_b128 v[194:197], v171 offset:21504
	ds_read_b128 v[204:207], v171 offset:22528
	ds_read_b128 v[208:211], v171 offset:23552
	buffer_load_dwordx4 v164, s[4:7], s14 offen lds
	s_mov_b32 m0, s10
	s_add_i32 s63, s14, 0x40000
	buffer_load_dwordx4 v166, s[4:7], s14 offen lds
	s_mov_b32 m0, s11
	s_nop 0
	buffer_load_dwordx4 v164, s[4:7], s63 offen lds
	s_mov_b32 m0, s12
	s_nop 0
	buffer_load_dwordx4 v166, s[4:7], s63 offen lds
	s_waitcnt vmcnt(6)
	s_waitcnt lgkmcnt(0)
	s_barrier
	s_setprio 1
	s_cmp_eq_u32 s32, 1
	s_cbranch_scc1 .Lhk_5
	s_waitcnt lgkmcnt(6)
	v_mfma_scale_f32_16x16x128_f8f6f4 v[86:89], v[2:9], v[174:181], v[86:89], v234, v234 op_sel_hi:[0,0,0]
	v_mfma_scale_f32_16x16x128_f8f6f4 v[82:85], v[10:17], v[174:181], v[82:85], v234, v234 op_sel_hi:[0,0,0]
	s_waitcnt lgkmcnt(4)
	v_mfma_scale_f32_16x16x128_f8f6f4 v[70:73], v[2:9], v[182:189], v[70:73], v234, v234 op_sel_hi:[0,0,0]
	v_mfma_scale_f32_16x16x128_f8f6f4 v[66:69], v[10:17], v[182:189], v[66:69], v234, v234 op_sel_hi:[0,0,0]
	s_waitcnt lgkmcnt(2)
	v_mfma_scale_f32_16x16x128_f8f6f4 v[58:61], v[2:9], v[190:197], v[58:61], v234, v234 op_sel_hi:[0,0,0]
	v_mfma_scale_f32_16x16x128_f8f6f4 v[50:53], v[10:17], v[190:197], v[50:53], v234, v234 op_sel_hi:[0,0,0]
	s_waitcnt lgkmcnt(0)
	v_mfma_scale_f32_16x16x128_f8f6f4 v[42:45], v[2:9], v[204:211], v[42:45], v234, v234 op_sel_hi:[0,0,0]
	v_mfma_scale_f32_16x16x128_f8f6f4 v[34:37], v[10:17], v[204:211], v[34:37], v234, v234 op_sel_hi:[0,0,0]
	v_mfma_scale_f32_16x16x128_f8f6f4 v[102:105], v[18:25], v[174:181], v[102:105], v234, v234 op_sel_hi:[0,0,0]
	v_mfma_scale_f32_16x16x128_f8f6f4 v[94:97], v[26:33], v[174:181], v[94:97], v234, v234 op_sel_hi:[0,0,0]
	v_mfma_scale_f32_16x16x128_f8f6f4 v[78:81], v[18:25], v[182:189], v[78:81], v234, v234 op_sel_hi:[0,0,0]
	v_mfma_scale_f32_16x16x128_f8f6f4 v[74:77], v[26:33], v[182:189], v[74:77], v234, v234 op_sel_hi:[0,0,0]
	v_mfma_scale_f32_16x16x128_f8f6f4 v[62:65], v[18:25], v[190:197], v[62:65], v234, v234 op_sel_hi:[0,0,0]
	v_mfma_scale_f32_16x16x128_f8f6f4 v[54:57], v[26:33], v[190:197], v[54:57], v234, v234 op_sel_hi:[0,0,0]
	v_mfma_scale_f32_16x16x128_f8f6f4 v[46:49], v[18:25], v[204:211], v[46:49], v234, v234 op_sel_hi:[0,0,0]
	v_mfma_scale_f32_16x16x128_f8f6f4 v[38:41], v[26:33], v[204:211], v[38:41], v234, v234 op_sel_hi:[0,0,0]
.Lhk_5:
	s_setprio 0
	s_barrier
	ds_read_b128 v[18:21], v172
	ds_read_b128 v[22:25], v172 offset:1024
	ds_read_b128 v[26:29], v172 offset:2048
	ds_read_b128 v[30:33], v172 offset:3072
	ds_read_b128 v[10:13], v173
	ds_read_b128 v[14:17], v173 offset:1024
	ds_read_b128 v[2:5], v173 offset:2048
	ds_read_b128 v[6:9], v173 offset:3072
	s_mov_b32 m0, s8
	ds_read_b128 v[174:177], v171 offset:32768
	ds_read_b128 v[178:181], v171 offset:33792
	ds_read_b128 v[182:185], v171 offset:34816
	ds_read_b128 v[186:189], v171 offset:35840
	ds_read_b128 v[190:193], v171 offset:36864
	ds_read_b128 v[194:197], v171 offset:37888
	ds_read_b128 v[204:207], v171 offset:38912
	ds_read_b128 v[208:211], v171 offset:39936
	buffer_load_dwordx4 v163, s[64:67], s15 offen lds
	s_mov_b32 m0, s13
	s_nop 0
	buffer_load_dwordx4 v165, s[64:67], s15 offen lds
	s_add_i32 s15, s15, 0x40000
	s_mov_b32 m0, s20
	s_nop 0
	buffer_load_dwordx4 v163, s[64:67], s15 offen lds
	s_mov_b32 m0, s21
	s_nop 0
	buffer_load_dwordx4 v165, s[64:67], s15 offen lds
	s_waitcnt vmcnt(8)
	s_waitcnt lgkmcnt(0)
	s_barrier
	s_setprio 1
	s_cmp_eq_u32 s32, 2
	s_cbranch_scc1 .Lhk_6
	s_waitcnt lgkmcnt(6)
	v_mfma_scale_f32_16x16x128_f8f6f4 v[150:153], v[18:25], v[174:181], v[150:153], v234, v234 op_sel_hi:[0,0,0]
	v_mfma_scale_f32_16x16x128_f8f6f4 v[146:149], v[26:33], v[174:181], v[146:149], v234, v234 op_sel_hi:[0,0,0]
	s_waitcnt lgkmcnt(4)
	v_mfma_scale_f32_16x16x128_f8f6f4 v[134:137], v[18:25], v[182:189], v[134:137], v234, v234 op_sel_hi:[0,0,0]
	v_mfma_scale_f32_16x16x128_f8f6f4 v[130:133], v[26:33], v[182:189], v[130:133], v234, v234 op_sel_hi:[0,0,0]
	s_waitcnt lgkmcnt(2)
	v_mfma_scale_f32_16x16x128_f8f6f4 v[118:121], v[18:25], v[190:197], v[118:121], v234, v234 op_sel_hi:[0,0,0]
	v_mfma_scale_f32_16x16x128_f8f6f4 v[114:117], v[26:33], v[190:197], v[114:117], v234, v234 op_sel_hi:[0,0,0]
	s_waitcnt lgkmcnt(0)
	v_mfma_scale_f32_16x16x128_f8f6f4 v[98:101], v[18:25], v[204:211], v[98:101], v234, v234 op_sel_hi:[0,0,0]
	v_mfma_scale_f32_16x16x128_f8f6f4 v[90:93], v[26:33], v[204:211], v[90:93], v234, v234 op_sel_hi:[0,0,0]
	v_mfma_scale_f32_16x16x128_f8f6f4 v[158:161], v[10:17], v[174:181], v[158:161], v234, v234 op_sel_hi:[0,0,0]
	v_mfma_scale_f32_16x16x128_f8f6f4 v[154:157], v[2:9], v[174:181], v[154:157], v234, v234 op_sel_hi:[0,0,0]
	v_mfma_scale_f32_16x16x128_f8f6f4 v[142:145], v[10:17], v[182:189], v[142:145], v234, v234 op_sel_hi:[0,0,0]
	v_mfma_scale_f32_16x16x128_f8f6f4 v[138:141], v[2:9], v[182:189], v[138:141], v234, v234 op_sel_hi:[0,0,0]
	v_mfma_scale_f32_16x16x128_f8f6f4 v[126:129], v[10:17], v[190:197], v[126:129], v234, v234 op_sel_hi:[0,0,0]
	v_mfma_scale_f32_16x16x128_f8f6f4 v[122:125], v[2:9], v[190:197], v[122:125], v234, v234 op_sel_hi:[0,0,0]
	v_mfma_scale_f32_16x16x128_f8f6f4 v[110:113], v[10:17], v[204:211], v[110:113], v234, v234 op_sel_hi:[0,0,0]
	v_mfma_scale_f32_16x16x128_f8f6f4 v[106:109], v[2:9], v[204:211], v[106:109], v234, v234 op_sel_hi:[0,0,0]
.Lhk_6:
	s_setprio 0
	s_barrier
	s_mov_b32 m0, s26
	s_or_b32 s15, s14, 0x80
	ds_read_b128 v[174:177], v171 offset:49152
	ds_read_b128 v[178:181], v171 offset:50176
	ds_read_b128 v[182:185], v171 offset:51200
	ds_read_b128 v[186:189], v171 offset:52224
	ds_read_b128 v[190:193], v171 offset:53248
	ds_read_b128 v[194:197], v171 offset:54272
	ds_read_b128 v[204:207], v171 offset:55296
	ds_read_b128 v[208:211], v171 offset:56320
	buffer_load_dwordx4 v164, s[4:7], s15 offen lds
	s_mov_b32 m0, s27
	s_add_i32 s14, s14, 0x40080
	buffer_load_dwordx4 v166, s[4:7], s15 offen lds
	s_mov_b32 m0, s40
	s_nop 0
	buffer_load_dwordx4 v164, s[4:7], s14 offen lds
	s_mov_b32 m0, s76
	s_nop 0
	buffer_load_dwordx4 v166, s[4:7], s14 offen lds
	s_waitcnt vmcnt(6)
	s_waitcnt lgkmcnt(0)
	s_barrier
	s_setprio 1
	s_cmp_eq_u32 s32, 1
	s_cbranch_scc1 .Lhk_7
	s_waitcnt lgkmcnt(6)
	v_mfma_scale_f32_16x16x128_f8f6f4 v[86:89], v[18:25], v[174:181], v[86:89], v234, v234 op_sel_hi:[0,0,0]
	v_mfma_scale_f32_16x16x128_f8f6f4 v[82:85], v[26:33], v[174:181], v[82:85], v234, v234 op_sel_hi:[0,0,0]
	s_waitcnt lgkmcnt(4)
	v_mfma_scale_f32_16x16x128_f8f6f4 v[70:73], v[18:25], v[182:189], v[70:73], v234, v234 op_sel_hi:[0,0,0]
	v_mfma_scale_f32_16x16x128_f8f6f4 v[66:69], v[26:33], v[182:189], v[66:69], v234, v234 op_sel_hi:[0,0,0]
	s_waitcnt lgkmcnt(2)
	v_mfma_scale_f32_16x16x128_f8f6f4 v[58:61], v[18:25], v[190:197], v[58:61], v234, v234 op_sel_hi:[0,0,0]
	v_mfma_scale_f32_16x16x128_f8f6f4 v[50:53], v[26:33], v[190:197], v[50:53], v234, v234 op_sel_hi:[0,0,0]
	s_waitcnt lgkmcnt(0)
	v_mfma_scale_f32_16x16x128_f8f6f4 v[42:45], v[18:25], v[204:211], v[42:45], v234, v234 op_sel_hi:[0,0,0]
	v_mfma_scale_f32_16x16x128_f8f6f4 v[34:37], v[26:33], v[204:211], v[34:37], v234, v234 op_sel_hi:[0,0,0]
	v_mfma_scale_f32_16x16x128_f8f6f4 v[102:105], v[10:17], v[174:181], v[102:105], v234, v234 op_sel_hi:[0,0,0]
	v_mfma_scale_f32_16x16x128_f8f6f4 v[94:97], v[2:9], v[174:181], v[94:97], v234, v234 op_sel_hi:[0,0,0]
	v_mfma_scale_f32_16x16x128_f8f6f4 v[78:81], v[10:17], v[182:189], v[78:81], v234, v234 op_sel_hi:[0,0,0]
	v_mfma_scale_f32_16x16x128_f8f6f4 v[74:77], v[2:9], v[182:189], v[74:77], v234, v234 op_sel_hi:[0,0,0]
	v_mfma_scale_f32_16x16x128_f8f6f4 v[62:65], v[10:17], v[190:197], v[62:65], v234, v234 op_sel_hi:[0,0,0]
	v_mfma_scale_f32_16x16x128_f8f6f4 v[54:57], v[2:9], v[190:197], v[54:57], v234, v234 op_sel_hi:[0,0,0]
	v_mfma_scale_f32_16x16x128_f8f6f4 v[46:49], v[10:17], v[204:211], v[46:49], v234, v234 op_sel_hi:[0,0,0]
	v_mfma_scale_f32_16x16x128_f8f6f4 v[38:41], v[2:9], v[204:211], v[38:41], v234, v234 op_sel_hi:[0,0,0]
.Lhk_7:
	s_setprio 0
	s_barrier
	s_add_i32 s62, s62, 2
	s_addk_i32 s28, 0x100
	s_addk_i32 s29, 0x100
	s_cmp_gt_u32 s62, 13
	s_cbranch_scc0 .LBB0_225
	s_nop 15
	s_nop 15
	s_and_b64 vcc, exec, s[36:37]
	s_cbranch_vccz .LBB0_228
	s_barrier
.LBB0_228:
	v_mov_b32_e32 v3, v168
	v_mov_b32_e32 v4, v167
	v_exp_f32_e64 v5, -v150
	v_exp_f32_e64 v7, -v151
	s_lshl_b32 s7, s23, 8
	s_lshl_b32 s6, s84, 7
	v_lshlrev_b32_e32 v2, 4, v3
	v_lshlrev_b32_e32 v3, 3, v3
	v_and_or_b32 v2, v2, 16, s6
	s_mov_b32 s6, 0x3e38aa3b
	v_and_b32_e32 v3, -16, v3
	s_add_i32 s7, s7, s77
	v_add3_u32 v6, s7, v4, v3
	v_fma_f32 v4, v5, s6, s6
	v_fma_f32 v5, v7, s6, s6
	v_exp_f32_e64 v7, -v153
	v_exp_f32_e64 v8, -v152
	v_rcp_f32_e32 v4, v4
	v_rcp_f32_e32 v5, v5
	v_fma_f32 v7, v7, s6, s6
	v_fma_f32 v8, v8, s6, s6
	v_rcp_f32_e32 v9, v7
	v_exp_f32_e64 v7, -v146
	v_rcp_f32_e32 v8, v8
	v_pk_mul_f32 v[10:11], v[152:153], v[160:161]
	v_pk_mul_f32 v[12:13], v[150:151], v[158:159]
	v_fma_f32 v7, v7, s6, s6
	v_pk_mul_f32 v[10:11], v[10:11], v[8:9]
	v_pk_mul_f32 v[4:5], v[12:13], v[4:5]
	v_exp_f32_e64 v8, -v147
	v_exp_f32_e64 v9, -v148
	v_rcp_f32_e32 v12, v7
	v_exp_f32_e64 v7, -v149
	v_fma_f32 v13, v8, s6, s6
	v_fma_f32 v8, v9, s6, s6
	v_rcp_f32_e32 v8, v8
	v_fma_f32 v7, v7, s6, s6
	v_rcp_f32_e32 v9, v7
	v_pk_mul_f32 v[14:15], v[148:149], v[156:157]
	v_rcp_f32_e32 v13, v13
	v_med3_f32 v4, v4, s33, v236
	v_pk_mul_f32 v[14:15], v[14:15], v[8:9]
	v_med3_f32 v5, v5, s33, v236
	v_mov_b32_e32 v8, v1
	v_cvt_pk_fp8_f32 v8, v4, v5
	v_pk_mul_f32 v[16:17], v[146:147], v[154:155]
	v_med3_f32 v7, v10, s33, v236
	v_pk_mul_f32 v[4:5], v[16:17], v[12:13]
	v_med3_f32 v9, v11, s33, v236
	v_cvt_pk_fp8_f32 v8, v7, v9 op_sel:[0,0,1]
	v_med3_f32 v4, v4, s33, v236
	v_med3_f32 v5, v5, s33, v236
	v_mov_b32_e32 v9, v1
	v_cvt_pk_fp8_f32 v9, v4, v5
	v_med3_f32 v4, v14, s33, v236
	v_med3_f32 v7, v15, s33, v236
	v_exp_f32_e64 v5, -v134
	v_cvt_pk_fp8_f32 v9, v4, v7 op_sel:[0,0,1]
	v_exp_f32_e64 v7, -v135
	v_exp_f32_e64 v10, -v136
	v_fma_f32 v4, v5, s6, s6
	v_rcp_f32_e32 v4, v4
	v_fma_f32 v5, v7, s6, s6
	v_exp_f32_e64 v7, -v137
	v_fma_f32 v10, v10, s6, s6
	v_rcp_f32_e32 v10, v10
	v_rcp_f32_e32 v5, v5
	v_fma_f32 v7, v7, s6, s6
	v_rcp_f32_e32 v11, v7
	v_exp_f32_e64 v7, -v130
	v_pk_mul_f32 v[12:13], v[136:137], v[144:145]
	v_pk_mul_f32 v[14:15], v[134:135], v[142:143]
	v_pk_mul_f32 v[10:11], v[12:13], v[10:11]
	v_fma_f32 v7, v7, s6, s6
	v_exp_f32_e64 v13, -v131
	v_pk_mul_f32 v[4:5], v[14:15], v[4:5]
	v_exp_f32_e64 v14, -v132
	v_rcp_f32_e32 v12, v7
	v_exp_f32_e64 v7, -v133
	v_fma_f32 v13, v13, s6, s6
	v_fma_f32 v14, v14, s6, s6
	v_rcp_f32_e32 v13, v13
	v_fma_f32 v7, v7, s6, s6
	v_rcp_f32_e32 v14, v14
	v_rcp_f32_e32 v15, v7
	v_pk_mul_f32 v[18:19], v[130:131], v[138:139]
	v_pk_mul_f32 v[16:17], v[132:133], v[140:141]
	v_pk_mul_f32 v[12:13], v[18:19], v[12:13]
	v_med3_f32 v4, v4, s33, v236
	v_med3_f32 v5, v5, s33, v236
	v_med3_f32 v7, v10, s33, v236
	v_mov_b32_e32 v10, v1
	v_pk_mul_f32 v[14:15], v[16:17], v[14:15]
	v_med3_f32 v16, v11, s33, v236
	v_cvt_pk_fp8_f32 v10, v4, v5
	v_med3_f32 v4, v12, s33, v236
	v_med3_f32 v5, v13, s33, v236
	v_mov_b32_e32 v11, v1
	v_cvt_pk_fp8_f32 v11, v4, v5
	v_med3_f32 v4, v14, s33, v236
	v_med3_f32 v5, v15, s33, v236
	v_cvt_pk_fp8_f32 v10, v7, v16 op_sel:[0,0,1]
	v_cvt_pk_fp8_f32 v11, v4, v5 op_sel:[0,0,1]
	v_exp_f32_e64 v7, -v118
	v_or_b32_e32 v2, s78, v2
	v_mov_b64_e32 v[4:5], s[34:35]
	s_movk_i32 s7, 0x1600
	v_ashrrev_i32_e32 v3, 31, v2
	v_mad_i64_i32 v[12:13], s[14:15], v6, s7, v[4:5]
	v_permlane32_swap_b32_e32 v8, v10
	v_permlane32_swap_b32_e32 v9, v11
	v_lshl_add_u64 v[12:13], v[12:13], 0, v[2:3]
	v_fma_f32 v7, v7, s6, s6
	s_cmp_eq_u32 s32, 2
	s_cbranch_scc1 .Lhst_0
	global_store_dwordx4 v[12:13], v[8:11], off
.Lhst_0:
	v_pk_mul_f32 v[12:13], v[120:121], v[128:129]
	v_pk_mul_f32 v[14:15], v[118:119], v[126:127]
	v_rcp_f32_e32 v8, v7
	v_exp_f32_e64 v7, -v120
	v_exp_f32_e64 v11, -v121
	v_exp_f32_e64 v9, -v119
	v_pk_mul_f32 v[18:19], v[114:115], v[122:123]
	v_fma_f32 v7, v7, s6, s6
	v_rcp_f32_e32 v10, v7
	v_fma_f32 v7, v11, s6, s6
	v_rcp_f32_e32 v11, v7
	v_exp_f32_e64 v7, -v114
	v_fma_f32 v9, v9, s6, s6
	v_rcp_f32_e32 v9, v9
	v_pk_mul_f32 v[10:11], v[12:13], v[10:11]
	v_fma_f32 v7, v7, s6, s6
	v_exp_f32_e64 v13, -v115
	v_rcp_f32_e32 v12, v7
	v_exp_f32_e64 v7, -v117
	v_pk_mul_f32 v[8:9], v[14:15], v[8:9]
	v_exp_f32_e64 v14, -v116
	v_fma_f32 v13, v13, s6, s6
	v_fma_f32 v7, v7, s6, s6
	v_rcp_f32_e32 v15, v7
	v_rcp_f32_e32 v13, v13
	v_med3_f32 v7, v8, s33, v236
	v_med3_f32 v9, v9, s33, v236
	v_mov_b32_e32 v8, v1
	v_cvt_pk_fp8_f32 v8, v7, v9
	v_fma_f32 v14, v14, s6, s6
	v_rcp_f32_e32 v14, v14
	v_pk_mul_f32 v[12:13], v[18:19], v[12:13]
	v_med3_f32 v7, v10, s33, v236
	v_med3_f32 v9, v11, s33, v236
	v_cvt_pk_fp8_f32 v8, v7, v9 op_sel:[0,0,1]
	v_med3_f32 v7, v12, s33, v236
	v_med3_f32 v10, v13, s33, v236
	v_mov_b32_e32 v9, v1
	v_cvt_pk_fp8_f32 v9, v7, v10
	v_pk_mul_f32 v[16:17], v[116:117], v[124:125]
	v_exp_f32_e64 v12, -v100
	v_pk_mul_f32 v[14:15], v[16:17], v[14:15]
	v_exp_f32_e64 v13, -v101
	v_med3_f32 v7, v14, s33, v236
	v_med3_f32 v11, v15, s33, v236
	v_cvt_pk_fp8_f32 v9, v7, v11 op_sel:[0,0,1]
	v_exp_f32_e64 v7, -v99
	v_exp_f32_e64 v10, -v98
	v_pk_mul_f32 v[14:15], v[100:101], v[112:113]
	v_pk_mul_f32 v[16:17], v[98:99], v[110:111]
	v_fma_f32 v7, v7, s6, s6
	v_rcp_f32_e32 v11, v7
	v_fma_f32 v7, v12, s6, s6
	v_rcp_f32_e32 v12, v7
	v_fma_f32 v7, v13, s6, s6
	v_rcp_f32_e32 v13, v7
	v_fma_f32 v10, v10, s6, s6
	v_exp_f32_e64 v7, -v90
	v_rcp_f32_e32 v10, v10
	v_pk_mul_f32 v[12:13], v[14:15], v[12:13]
	v_exp_f32_e64 v15, -v91
	v_fma_f32 v7, v7, s6, s6
	v_pk_mul_f32 v[10:11], v[16:17], v[10:11]
	v_exp_f32_e64 v16, -v92
	v_rcp_f32_e32 v14, v7
	v_exp_f32_e64 v7, -v93
	v_fma_f32 v15, v15, s6, s6
	v_rcp_f32_e32 v15, v15
	v_fma_f32 v16, v16, s6, s6
	v_fma_f32 v7, v7, s6, s6
	v_pk_mul_f32 v[20:21], v[90:91], v[106:107]
	v_rcp_f32_e32 v16, v16
	v_rcp_f32_e32 v17, v7
	v_pk_mul_f32 v[14:15], v[20:21], v[14:15]
	v_med3_f32 v7, v10, s33, v236
	v_med3_f32 v11, v11, s33, v236
	v_mov_b32_e32 v10, v1
	v_cvt_pk_fp8_f32 v10, v7, v11
	v_med3_f32 v7, v14, s33, v236
	v_med3_f32 v14, v15, s33, v236
	v_mov_b32_e32 v11, v1
	v_cvt_pk_fp8_f32 v11, v7, v14
	v_pk_mul_f32 v[18:19], v[92:93], v[108:109]
	v_med3_f32 v12, v12, s33, v236
	v_pk_mul_f32 v[16:17], v[18:19], v[16:17]
	v_med3_f32 v13, v13, s33, v236
	v_cvt_pk_fp8_f32 v10, v12, v13 op_sel:[0,0,1]
	v_med3_f32 v7, v16, s33, v236
	v_med3_f32 v12, v17, s33, v236
	v_cvt_pk_fp8_f32 v11, v7, v12 op_sel:[0,0,1]
	v_add_u32_e32 v7, 32, v6
	v_mad_i64_i32 v[12:13], s[14:15], v7, s7, v[4:5]
	v_exp_f32_e64 v7, -v86
	v_permlane32_swap_b32_e32 v8, v10
	v_permlane32_swap_b32_e32 v9, v11
	v_lshl_add_u64 v[12:13], v[12:13], 0, v[2:3]
	v_fma_f32 v7, v7, s6, s6
	s_cmp_eq_u32 s32, 2
	s_cbranch_scc1 .Lhst_1
	global_store_dwordx4 v[12:13], v[8:11], off
.Lhst_1:
	v_pk_mul_f32 v[12:13], v[88:89], v[104:105]
	v_pk_mul_f32 v[14:15], v[86:87], v[102:103]
	v_rcp_f32_e32 v8, v7
	v_exp_f32_e64 v7, -v88
	v_exp_f32_e64 v11, -v89
	v_exp_f32_e64 v9, -v87
	v_pk_mul_f32 v[18:19], v[82:83], v[94:95]
	v_fma_f32 v7, v7, s6, s6
	v_rcp_f32_e32 v10, v7
	v_fma_f32 v7, v11, s6, s6
	v_rcp_f32_e32 v11, v7
	v_exp_f32_e64 v7, -v82
	v_fma_f32 v9, v9, s6, s6
	v_rcp_f32_e32 v9, v9
	v_pk_mul_f32 v[10:11], v[12:13], v[10:11]
	v_fma_f32 v7, v7, s6, s6
	v_exp_f32_e64 v13, -v83
	v_rcp_f32_e32 v12, v7
	v_exp_f32_e64 v7, -v85
	v_pk_mul_f32 v[8:9], v[14:15], v[8:9]
	v_exp_f32_e64 v14, -v84
	v_fma_f32 v13, v13, s6, s6
	v_fma_f32 v7, v7, s6, s6
	v_rcp_f32_e32 v15, v7
	v_rcp_f32_e32 v13, v13
	v_med3_f32 v7, v8, s33, v236
	v_med3_f32 v9, v9, s33, v236
	v_mov_b32_e32 v8, v1
	v_cvt_pk_fp8_f32 v8, v7, v9
	v_fma_f32 v14, v14, s6, s6
	v_rcp_f32_e32 v14, v14
	v_pk_mul_f32 v[12:13], v[18:19], v[12:13]
	v_med3_f32 v7, v10, s33, v236
	v_med3_f32 v9, v11, s33, v236
	v_cvt_pk_fp8_f32 v8, v7, v9 op_sel:[0,0,1]
	v_med3_f32 v7, v12, s33, v236
	v_med3_f32 v10, v13, s33, v236
	v_mov_b32_e32 v9, v1
	v_cvt_pk_fp8_f32 v9, v7, v10
	v_pk_mul_f32 v[16:17], v[84:85], v[96:97]
	v_exp_f32_e64 v12, -v72
	v_pk_mul_f32 v[14:15], v[16:17], v[14:15]
	v_exp_f32_e64 v13, -v73
	v_med3_f32 v7, v14, s33, v236
	v_med3_f32 v11, v15, s33, v236
	v_cvt_pk_fp8_f32 v9, v7, v11 op_sel:[0,0,1]
	v_exp_f32_e64 v7, -v71
	v_exp_f32_e64 v10, -v70
	v_pk_mul_f32 v[14:15], v[72:73], v[80:81]
	v_pk_mul_f32 v[16:17], v[70:71], v[78:79]
	v_fma_f32 v7, v7, s6, s6
	v_rcp_f32_e32 v11, v7
	v_fma_f32 v7, v12, s6, s6
	v_rcp_f32_e32 v12, v7
	v_fma_f32 v7, v13, s6, s6
	v_rcp_f32_e32 v13, v7
	v_fma_f32 v10, v10, s6, s6
	v_exp_f32_e64 v7, -v66
	v_rcp_f32_e32 v10, v10
	v_pk_mul_f32 v[12:13], v[14:15], v[12:13]
	v_exp_f32_e64 v15, -v67
	v_fma_f32 v7, v7, s6, s6
	v_pk_mul_f32 v[10:11], v[16:17], v[10:11]
	v_exp_f32_e64 v16, -v68
	v_rcp_f32_e32 v14, v7
	v_exp_f32_e64 v7, -v69
	v_fma_f32 v15, v15, s6, s6
	v_rcp_f32_e32 v15, v15
	v_fma_f32 v16, v16, s6, s6
	v_fma_f32 v7, v7, s6, s6
	v_pk_mul_f32 v[20:21], v[66:67], v[74:75]
	v_rcp_f32_e32 v16, v16
	v_rcp_f32_e32 v17, v7
	v_pk_mul_f32 v[14:15], v[20:21], v[14:15]
	v_med3_f32 v7, v10, s33, v236
	v_med3_f32 v11, v11, s33, v236
	v_mov_b32_e32 v10, v1
	v_cvt_pk_fp8_f32 v10, v7, v11
	v_med3_f32 v7, v14, s33, v236
	v_med3_f32 v14, v15, s33, v236
	v_mov_b32_e32 v11, v1
	v_cvt_pk_fp8_f32 v11, v7, v14
	v_pk_mul_f32 v[18:19], v[68:69], v[76:77]
	v_med3_f32 v12, v12, s33, v236
	v_pk_mul_f32 v[16:17], v[18:19], v[16:17]
	v_med3_f32 v13, v13, s33, v236
	v_cvt_pk_fp8_f32 v10, v12, v13 op_sel:[0,0,1]
	v_med3_f32 v7, v16, s33, v236
	v_med3_f32 v12, v17, s33, v236
	v_cvt_pk_fp8_f32 v11, v7, v12 op_sel:[0,0,1]
	v_exp_f32_e64 v7, -v58
	v_add_u32_e32 v22, 0x80, v6
	v_mad_i64_i32 v[12:13], s[14:15], v22, s7, v[4:5]
	v_permlane32_swap_b32_e32 v8, v10
	v_permlane32_swap_b32_e32 v9, v11
	v_lshl_add_u64 v[12:13], v[12:13], 0, v[2:3]
	v_fma_f32 v7, v7, s6, s6
	s_cmp_eq_u32 s32, 1
	s_cbranch_scc1 .Lhst_2
	global_store_dwordx4 v[12:13], v[8:11], off
.Lhst_2:
	v_pk_mul_f32 v[12:13], v[60:61], v[64:65]
	v_pk_mul_f32 v[14:15], v[58:59], v[62:63]
	v_rcp_f32_e32 v8, v7
	v_exp_f32_e64 v7, -v60
	v_exp_f32_e64 v11, -v61
	v_exp_f32_e64 v9, -v59
	v_pk_mul_f32 v[18:19], v[50:51], v[54:55]
	v_fma_f32 v7, v7, s6, s6
	v_rcp_f32_e32 v10, v7
	v_fma_f32 v7, v11, s6, s6
	v_rcp_f32_e32 v11, v7
	v_exp_f32_e64 v7, -v50
	v_fma_f32 v9, v9, s6, s6
	v_rcp_f32_e32 v9, v9
	v_pk_mul_f32 v[10:11], v[12:13], v[10:11]
	v_fma_f32 v7, v7, s6, s6
	v_exp_f32_e64 v13, -v51
	v_rcp_f32_e32 v12, v7
	v_exp_f32_e64 v7, -v53
	v_pk_mul_f32 v[8:9], v[14:15], v[8:9]
	v_exp_f32_e64 v14, -v52
	v_fma_f32 v13, v13, s6, s6
	v_fma_f32 v7, v7, s6, s6
	v_rcp_f32_e32 v15, v7
	v_rcp_f32_e32 v13, v13
	v_med3_f32 v7, v8, s33, v236
	v_med3_f32 v9, v9, s33, v236
	v_mov_b32_e32 v8, v1
	v_cvt_pk_fp8_f32 v8, v7, v9
	v_fma_f32 v14, v14, s6, s6
	v_rcp_f32_e32 v14, v14
	v_pk_mul_f32 v[12:13], v[18:19], v[12:13]
	v_med3_f32 v7, v10, s33, v236
	v_med3_f32 v9, v11, s33, v236
	v_cvt_pk_fp8_f32 v8, v7, v9 op_sel:[0,0,1]
	v_med3_f32 v7, v12, s33, v236
	v_med3_f32 v10, v13, s33, v236
	v_mov_b32_e32 v9, v1
	v_cvt_pk_fp8_f32 v9, v7, v10
	v_pk_mul_f32 v[16:17], v[52:53], v[56:57]
	v_exp_f32_e64 v12, -v44
	v_pk_mul_f32 v[14:15], v[16:17], v[14:15]
	v_exp_f32_e64 v13, -v45
	v_med3_f32 v7, v14, s33, v236
	v_med3_f32 v11, v15, s33, v236
	v_cvt_pk_fp8_f32 v9, v7, v11 op_sel:[0,0,1]
	v_exp_f32_e64 v7, -v43
	v_exp_f32_e64 v10, -v42
	v_pk_mul_f32 v[14:15], v[44:45], v[48:49]
	v_pk_mul_f32 v[16:17], v[42:43], v[46:47]
	v_fma_f32 v7, v7, s6, s6
	v_rcp_f32_e32 v11, v7
	v_fma_f32 v7, v12, s6, s6
	v_rcp_f32_e32 v12, v7
	v_fma_f32 v7, v13, s6, s6
	v_rcp_f32_e32 v13, v7
	v_fma_f32 v10, v10, s6, s6
	v_exp_f32_e64 v7, -v34
	v_rcp_f32_e32 v10, v10
	v_pk_mul_f32 v[12:13], v[14:15], v[12:13]
	v_exp_f32_e64 v15, -v35
	v_fma_f32 v7, v7, s6, s6
	v_pk_mul_f32 v[10:11], v[16:17], v[10:11]
	v_exp_f32_e64 v16, -v36
	v_rcp_f32_e32 v14, v7
	v_exp_f32_e64 v7, -v37
	v_fma_f32 v15, v15, s6, s6
	v_rcp_f32_e32 v15, v15
	v_fma_f32 v16, v16, s6, s6
	v_fma_f32 v7, v7, s6, s6
	v_pk_mul_f32 v[20:21], v[34:35], v[38:39]
	v_rcp_f32_e32 v16, v16
	v_rcp_f32_e32 v17, v7
	v_pk_mul_f32 v[14:15], v[20:21], v[14:15]
	v_med3_f32 v7, v10, s33, v236
	v_med3_f32 v11, v11, s33, v236
	v_mov_b32_e32 v10, v1
	v_cvt_pk_fp8_f32 v10, v7, v11
	v_med3_f32 v7, v14, s33, v236
	v_med3_f32 v14, v15, s33, v236
	v_mov_b32_e32 v11, v1
	v_cvt_pk_fp8_f32 v11, v7, v14
	v_pk_mul_f32 v[18:19], v[36:37], v[40:41]
	v_med3_f32 v12, v12, s33, v236
	v_pk_mul_f32 v[16:17], v[18:19], v[16:17]
	v_med3_f32 v13, v13, s33, v236
	v_cvt_pk_fp8_f32 v10, v12, v13 op_sel:[0,0,1]
	v_med3_f32 v7, v16, s33, v236
	v_med3_f32 v12, v17, s33, v236
	v_cvt_pk_fp8_f32 v11, v7, v12 op_sel:[0,0,1]
	v_add_u32_e32 v6, 0xa0, v6
	v_mad_i64_i32 v[4:5], s[6:7], v6, s7, v[4:5]
	s_mov_b32 s62, 0x41200000
	v_permlane32_swap_b32_e32 v8, v10
	v_permlane32_swap_b32_e32 v9, v11
	v_lshl_add_u64 v[2:3], v[4:5], 0, v[2:3]
	s_andn2_b64 vcc, exec, s[38:39]
	s_mov_b64 s[6:7], -1
	s_mov_b32 s63, 0x41300000
	s_cmp_eq_u32 s32, 1
	s_cbranch_scc1 .Lhst_3
	global_store_dwordx4 v[2:3], v[8:11], off
.Lhst_3:
	s_cbranch_vccnz .LBB0_221
	s_andn2_b64 vcc, exec, s[2:3]
	s_cbranch_vccnz .LBB0_220
	s_barrier
	s_branch .LBB0_220
